# baseline (speedup 1.0000x reference)
.LBB0_46:
	s_or_b64 exec, exec, s[4:5]
	v_lshlrev_b32_e32 v2, 5, v44
	s_waitcnt lgkmcnt(0)
	s_barrier
	ds_read_b128 v[14:17], v2 offset:20480
	ds_read_b128 v[2:5], v2 offset:20496
	v_mov_b32_e32 v41, 0
	v_lshlrev_b32_e32 v40, 4, v1
	s_waitcnt lgkmcnt(1)
	v_cmp_gt_i32_e64 s[16:17], 0, v14
	v_max_i32_e32 v42, 0, v14
	v_lshl_add_u32 v42, v42, 10, v40
	global_load_dwordx4 v[48:51], v42, s[24:25] nt
	v_cmp_gt_i32_e64 s[14:15], 0, v15
	v_max_i32_e32 v43, 0, v15
	v_lshl_add_u32 v43, v43, 10, v40
	global_load_dwordx4 v[34:37], v43, s[24:25] nt
	v_cmp_gt_i32_e64 s[12:13], 0, v16
	v_max_i32_e32 v42, 0, v16
	v_lshl_add_u32 v42, v42, 10, v40
	global_load_dwordx4 v[30:33], v42, s[24:25] nt
	v_cmp_gt_i32_e64 s[10:11], 0, v17
	v_max_i32_e32 v43, 0, v17
	v_lshl_add_u32 v43, v43, 10, v40
	global_load_dwordx4 v[26:29], v43, s[24:25] nt
	s_waitcnt lgkmcnt(0)
	v_cmp_gt_i32_e64 s[8:9], 0, v2
	v_max_i32_e32 v42, 0, v2
	v_lshl_add_u32 v42, v42, 10, v40
	global_load_dwordx4 v[22:25], v42, s[24:25] nt
	v_cmp_gt_i32_e64 s[6:7], 0, v3
	v_max_i32_e32 v43, 0, v3
	v_lshl_add_u32 v43, v43, 10, v40
	global_load_dwordx4 v[18:21], v43, s[24:25] nt
	v_cmp_gt_i32_e64 s[4:5], 0, v4
	v_max_i32_e32 v42, 0, v4
	v_lshl_add_u32 v42, v42, 10, v40
	global_load_dwordx4 v[10:13], v42, s[24:25] nt
	v_cmp_gt_i32_e64 s[2:3], 0, v5
	v_max_i32_e32 v43, 0, v5
	v_lshl_add_u32 v43, v43, 10, v40
	global_load_dwordx4 v[6:9], v43, s[24:25] nt
	v_lshlrev_b32_e32 v1, 8, v0
	v_lshlrev_b32_e32 v0, 3, v0
	s_movk_i32 s19, 0x3c00
	v_and_b32_e32 v0, 8, v0
	v_and_or_b32 v46, v1, s19, v0
	s_mul_i32 s18, s20, 0x4080
	s_mul_hi_u32 s24, s20, 0x4080
	s_add_u32 s18, s22, s18
	v_lshlrev_b32_e32 v39, 3, v44
	v_and_b32_e32 v41, 32, v38
	s_addc_u32 s19, s23, s24
	s_add_u32 s22, s18, 0x4000
	s_addc_u32 s23, s19, 0
	v_add_u32_e32 v60, v39, v41
	v_lshl_add_u32 v60, v60, 4, v46
	v_lshrrev_b32_e32 v67, 1, v40
	v_and_b32_e32 v67, 0x70, v67
	v_or_b32_e32 v67, v60, v67
	v_mov_b32_e32 v66, 0x7f800000
	s_waitcnt vmcnt(7)
	v_cndmask_b32_e64 v48, v48, 0, s[16:17]
	v_cndmask_b32_e64 v49, v49, 0, s[16:17]
	v_cndmask_b32_e64 v50, v50, 0, s[16:17]
	v_cndmask_b32_e64 v51, v51, 0, s[16:17]
	v_pk_mul_f32 v[62:63], v[48:49], v[48:49]
	v_pk_mul_f32 v[64:65], v[50:51], v[50:51]
	v_add_f32_e32 v52, v62, v63
	v_add_f32_e32 v52, v52, v64
	v_add_f32_e32 v52, v52, v65
	v_cvt_pk_f16_f32 v62, v48, v49
	v_cvt_pk_f16_f32 v63, v50, v51
	ds_write_b64 v67, v[62:63]
	s_waitcnt vmcnt(6)
	v_cndmask_b32_e64 v34, v34, 0, s[14:15]
	v_cndmask_b32_e64 v35, v35, 0, s[14:15]
	v_cndmask_b32_e64 v36, v36, 0, s[14:15]
	v_cndmask_b32_e64 v37, v37, 0, s[14:15]
	v_pk_mul_f32 v[62:63], v[34:35], v[34:35]
	v_pk_mul_f32 v[64:65], v[36:37], v[36:37]
	v_add_f32_e32 v53, v62, v63
	v_add_f32_e32 v53, v53, v64
	v_add_f32_e32 v53, v53, v65
	v_cvt_pk_f16_f32 v62, v34, v35
	v_cvt_pk_f16_f32 v63, v36, v37
	v_xor_b32_e32 v68, 0x10, v67
	ds_write_b64 v68, v[62:63]
	s_waitcnt vmcnt(5)
	v_cndmask_b32_e64 v30, v30, 0, s[12:13]
	v_cndmask_b32_e64 v31, v31, 0, s[12:13]
	v_cndmask_b32_e64 v32, v32, 0, s[12:13]
	v_cndmask_b32_e64 v33, v33, 0, s[12:13]
	v_pk_mul_f32 v[62:63], v[30:31], v[30:31]
	v_pk_mul_f32 v[64:65], v[32:33], v[32:33]
	v_add_f32_e32 v54, v62, v63
	v_add_f32_e32 v54, v54, v64
	v_add_f32_e32 v54, v54, v65
	v_cvt_pk_f16_f32 v62, v30, v31
	v_cvt_pk_f16_f32 v63, v32, v33
	v_xor_b32_e32 v68, 0x20, v67
	ds_write_b64 v68, v[62:63]
	s_waitcnt vmcnt(4)
	v_cndmask_b32_e64 v26, v26, 0, s[10:11]
	v_cndmask_b32_e64 v27, v27, 0, s[10:11]
	v_cndmask_b32_e64 v28, v28, 0, s[10:11]
	v_cndmask_b32_e64 v29, v29, 0, s[10:11]
	v_pk_mul_f32 v[62:63], v[26:27], v[26:27]
	v_pk_mul_f32 v[64:65], v[28:29], v[28:29]
	v_add_f32_e32 v55, v62, v63
	v_add_f32_e32 v55, v55, v64
	v_add_f32_e32 v55, v55, v65
	v_cvt_pk_f16_f32 v62, v26, v27
	v_cvt_pk_f16_f32 v63, v28, v29
	v_xor_b32_e32 v68, 0x30, v67
	ds_write_b64 v68, v[62:63]
	s_waitcnt vmcnt(3)
	v_cndmask_b32_e64 v22, v22, 0, s[8:9]
	v_cndmask_b32_e64 v23, v23, 0, s[8:9]
	v_cndmask_b32_e64 v24, v24, 0, s[8:9]
	v_cndmask_b32_e64 v25, v25, 0, s[8:9]
	v_pk_mul_f32 v[62:63], v[22:23], v[22:23]
	v_pk_mul_f32 v[64:65], v[24:25], v[24:25]
	v_add_f32_e32 v56, v62, v63
	v_add_f32_e32 v56, v56, v64
	v_add_f32_e32 v56, v56, v65
	v_cvt_pk_f16_f32 v62, v22, v23
	v_cvt_pk_f16_f32 v63, v24, v25
	v_xor_b32_e32 v68, 0x40, v67
	ds_write_b64 v68, v[62:63]
	s_waitcnt vmcnt(2)
	v_cndmask_b32_e64 v18, v18, 0, s[6:7]
	v_cndmask_b32_e64 v19, v19, 0, s[6:7]
	v_cndmask_b32_e64 v20, v20, 0, s[6:7]
	v_cndmask_b32_e64 v21, v21, 0, s[6:7]
	v_pk_mul_f32 v[62:63], v[18:19], v[18:19]
	v_pk_mul_f32 v[64:65], v[20:21], v[20:21]
	v_add_f32_e32 v57, v62, v63
	v_add_f32_e32 v57, v57, v64
	v_add_f32_e32 v57, v57, v65
	v_cvt_pk_f16_f32 v62, v18, v19
	v_cvt_pk_f16_f32 v63, v20, v21
	v_xor_b32_e32 v68, 0x50, v67
	ds_write_b64 v68, v[62:63]
	s_waitcnt vmcnt(1)
	v_cndmask_b32_e64 v10, v10, 0, s[4:5]
	v_cndmask_b32_e64 v11, v11, 0, s[4:5]
	v_cndmask_b32_e64 v12, v12, 0, s[4:5]
	v_cndmask_b32_e64 v13, v13, 0, s[4:5]
	v_pk_mul_f32 v[62:63], v[10:11], v[10:11]
	v_pk_mul_f32 v[64:65], v[12:13], v[12:13]
	v_add_f32_e32 v58, v62, v63
	v_add_f32_e32 v58, v58, v64
	v_add_f32_e32 v58, v58, v65
	v_cvt_pk_f16_f32 v62, v10, v11
	v_cvt_pk_f16_f32 v63, v12, v13
	v_xor_b32_e32 v68, 0x60, v67
	ds_write_b64 v68, v[62:63]
	s_waitcnt vmcnt(0)
	v_cndmask_b32_e64 v6, v6, 0, s[2:3]
	v_cndmask_b32_e64 v7, v7, 0, s[2:3]
	v_cndmask_b32_e64 v8, v8, 0, s[2:3]
	v_cndmask_b32_e64 v9, v9, 0, s[2:3]
	v_pk_mul_f32 v[62:63], v[6:7], v[6:7]
	v_pk_mul_f32 v[64:65], v[8:9], v[8:9]
	v_add_f32_e32 v59, v62, v63
	v_add_f32_e32 v59, v59, v64
	v_add_f32_e32 v59, v59, v65
	v_cvt_pk_f16_f32 v62, v6, v7
	v_cvt_pk_f16_f32 v63, v8, v9
	v_xor_b32_e32 v68, 0x70, v67
	ds_write_b64 v68, v[62:63]
	v_add_f32_dpp v52, v52, v52 quad_perm:[1,0,3,2] row_mask:0xf bank_mask:0xf bound_ctrl:1
	v_add_f32_dpp v53, v53, v53 quad_perm:[1,0,3,2] row_mask:0xf bank_mask:0xf bound_ctrl:1
	v_add_f32_dpp v54, v54, v54 quad_perm:[1,0,3,2] row_mask:0xf bank_mask:0xf bound_ctrl:1
	v_add_f32_dpp v55, v55, v55 quad_perm:[1,0,3,2] row_mask:0xf bank_mask:0xf bound_ctrl:1
	v_add_f32_dpp v56, v56, v56 quad_perm:[1,0,3,2] row_mask:0xf bank_mask:0xf bound_ctrl:1
	v_add_f32_dpp v57, v57, v57 quad_perm:[1,0,3,2] row_mask:0xf bank_mask:0xf bound_ctrl:1
	v_add_f32_dpp v58, v58, v58 quad_perm:[1,0,3,2] row_mask:0xf bank_mask:0xf bound_ctrl:1
	v_add_f32_dpp v59, v59, v59 quad_perm:[1,0,3,2] row_mask:0xf bank_mask:0xf bound_ctrl:1
	v_add_f32_dpp v52, v52, v52 quad_perm:[2,3,0,1] row_mask:0xf bank_mask:0xf bound_ctrl:1
	v_add_f32_dpp v53, v53, v53 quad_perm:[2,3,0,1] row_mask:0xf bank_mask:0xf bound_ctrl:1
	v_add_f32_dpp v54, v54, v54 quad_perm:[2,3,0,1] row_mask:0xf bank_mask:0xf bound_ctrl:1
	v_add_f32_dpp v55, v55, v55 quad_perm:[2,3,0,1] row_mask:0xf bank_mask:0xf bound_ctrl:1
	v_add_f32_dpp v56, v56, v56 quad_perm:[2,3,0,1] row_mask:0xf bank_mask:0xf bound_ctrl:1
	v_add_f32_dpp v57, v57, v57 quad_perm:[2,3,0,1] row_mask:0xf bank_mask:0xf bound_ctrl:1
	v_add_f32_dpp v58, v58, v58 quad_perm:[2,3,0,1] row_mask:0xf bank_mask:0xf bound_ctrl:1
	v_add_f32_dpp v59, v59, v59 quad_perm:[2,3,0,1] row_mask:0xf bank_mask:0xf bound_ctrl:1
	v_add_f32_dpp v52, v52, v52 row_half_mirror row_mask:0xf bank_mask:0xf bound_ctrl:1
	v_add_f32_dpp v53, v53, v53 row_half_mirror row_mask:0xf bank_mask:0xf bound_ctrl:1
	v_add_f32_dpp v54, v54, v54 row_half_mirror row_mask:0xf bank_mask:0xf bound_ctrl:1
	v_add_f32_dpp v55, v55, v55 row_half_mirror row_mask:0xf bank_mask:0xf bound_ctrl:1
	v_add_f32_dpp v56, v56, v56 row_half_mirror row_mask:0xf bank_mask:0xf bound_ctrl:1
	v_add_f32_dpp v57, v57, v57 row_half_mirror row_mask:0xf bank_mask:0xf bound_ctrl:1
	v_add_f32_dpp v58, v58, v58 row_half_mirror row_mask:0xf bank_mask:0xf bound_ctrl:1
	v_add_f32_dpp v59, v59, v59 row_half_mirror row_mask:0xf bank_mask:0xf bound_ctrl:1
	v_add_f32_dpp v52, v52, v52 row_mirror row_mask:0xf bank_mask:0xf bound_ctrl:1
	v_add_f32_dpp v53, v53, v53 row_mirror row_mask:0xf bank_mask:0xf bound_ctrl:1
	v_add_f32_dpp v54, v54, v54 row_mirror row_mask:0xf bank_mask:0xf bound_ctrl:1
	v_add_f32_dpp v55, v55, v55 row_mirror row_mask:0xf bank_mask:0xf bound_ctrl:1
	v_add_f32_dpp v56, v56, v56 row_mirror row_mask:0xf bank_mask:0xf bound_ctrl:1
	v_add_f32_dpp v57, v57, v57 row_mirror row_mask:0xf bank_mask:0xf bound_ctrl:1
	v_add_f32_dpp v58, v58, v58 row_mirror row_mask:0xf bank_mask:0xf bound_ctrl:1
	v_add_f32_dpp v59, v59, v59 row_mirror row_mask:0xf bank_mask:0xf bound_ctrl:1
	v_add_f32_dpp v52, v52, v52 row_bcast:15 row_mask:0xa bank_mask:0xf
	v_add_f32_dpp v53, v53, v53 row_bcast:15 row_mask:0xa bank_mask:0xf
	v_add_f32_dpp v54, v54, v54 row_bcast:15 row_mask:0xa bank_mask:0xf
	v_add_f32_dpp v55, v55, v55 row_bcast:15 row_mask:0xa bank_mask:0xf
	v_add_f32_dpp v56, v56, v56 row_bcast:15 row_mask:0xa bank_mask:0xf
	v_add_f32_dpp v57, v57, v57 row_bcast:15 row_mask:0xa bank_mask:0xf
	v_add_f32_dpp v58, v58, v58 row_bcast:15 row_mask:0xa bank_mask:0xf
	v_add_f32_dpp v59, v59, v59 row_bcast:15 row_mask:0xa bank_mask:0xf
	v_add_f32_dpp v52, v52, v52 row_bcast:31 row_mask:0xc bank_mask:0xf
	v_add_f32_dpp v53, v53, v53 row_bcast:31 row_mask:0xc bank_mask:0xf
	v_add_f32_dpp v54, v54, v54 row_bcast:31 row_mask:0xc bank_mask:0xf
	v_add_f32_dpp v55, v55, v55 row_bcast:31 row_mask:0xc bank_mask:0xf
	v_add_f32_dpp v56, v56, v56 row_bcast:31 row_mask:0xc bank_mask:0xf
	v_add_f32_dpp v57, v57, v57 row_bcast:31 row_mask:0xc bank_mask:0xf
	v_add_f32_dpp v58, v58, v58 row_bcast:31 row_mask:0xc bank_mask:0xf
	v_add_f32_dpp v59, v59, v59 row_bcast:31 row_mask:0xc bank_mask:0xf
	v_pk_add_f32 v[0:1], v[48:49], 0 op_sel_hi:[1,0]
	v_pk_add_f32 v[2:3], v[50:51], 0 op_sel_hi:[1,0]
	v_pk_add_f32 v[0:1], v[0:1], v[34:35]
	v_pk_add_f32 v[2:3], v[2:3], v[36:37]
	v_pk_add_f32 v[0:1], v[0:1], v[30:31]
	v_pk_add_f32 v[2:3], v[2:3], v[32:33]
	v_pk_add_f32 v[0:1], v[0:1], v[26:27]
	v_pk_add_f32 v[2:3], v[2:3], v[28:29]
	v_pk_add_f32 v[0:1], v[0:1], v[22:23]
	v_pk_add_f32 v[2:3], v[2:3], v[24:25]
	v_pk_add_f32 v[0:1], v[0:1], v[18:19]
	v_pk_add_f32 v[2:3], v[2:3], v[20:21]
	v_pk_add_f32 v[0:1], v[0:1], v[10:11]
	v_pk_add_f32 v[2:3], v[2:3], v[12:13]
	v_pk_add_f32 v[0:1], v[0:1], v[6:7]
	v_pk_add_f32 v[2:3], v[2:3], v[8:9]
	s_mov_b64 s[24:25], exec
	s_mov_b32 exec_lo, 0
	s_brev_b32 exec_hi, 1
	v_cndmask_b32_e64 v52, v52, v66, s[16:17]
	v_cndmask_b32_e64 v53, v53, v66, s[14:15]
	v_cndmask_b32_e64 v54, v54, v66, s[12:13]
	v_cndmask_b32_e64 v55, v55, v66, s[10:11]
	v_cndmask_b32_e64 v56, v56, v66, s[8:9]
	v_cndmask_b32_e64 v57, v57, v66, s[6:7]
	v_cndmask_b32_e64 v58, v58, v66, s[4:5]
	v_cndmask_b32_e64 v59, v59, v66, s[2:3]
	v_lshlrev_b32_e32 v61, 2, v39
	global_store_dwordx4 v61, v[52:55], s[22:23]
	global_store_dwordx4 v61, v[56:59], s[22:23] offset:16
	s_mov_b64 exec, s[24:25]
	s_load_dwordx2 s[6:7], s[0:1], 0x18
	v_lshl_or_b32 v4, v44, 10, v40
	ds_write_b128 v4, v[0:3] offset:16384
	s_waitcnt lgkmcnt(0)
	s_barrier
	v_lshrrev_b32_e32 v12, 5, v38
	v_and_b32_e32 v12, 0x70, v12
	v_xor_b32_e32 v12, v38, v12
	ds_read_b128 v[0:3], v12
	ds_read_b128 v[4:7], v12 offset:4096
	v_mov_b32_e32 v39, 0
	v_lshl_add_u64 v[8:9], s[18:19], 0, v[38:39]
	s_movk_i32 s0, 0x2000
	s_waitcnt lgkmcnt(1)
	global_store_dwordx4 v38, v[0:3], s[18:19]
	ds_read_b128 v[0:3], v12 offset:8192
	v_add_co_u32_e32 v10, vcc, s0, v8
	s_movk_i32 s0, 0x3000
	s_nop 0
	v_addc_co_u32_e32 v11, vcc, 0, v9, vcc
	s_waitcnt lgkmcnt(1)
	global_store_dwordx4 v[10:11], v[4:7], off offset:-4096
	ds_read_b128 v[4:7], v12 offset:12288
	s_waitcnt lgkmcnt(1)
	global_store_dwordx4 v[10:11], v[0:3], off
	ds_read2st64_b32 v[0:1], v45 offset0:64 offset1:68
	ds_read2st64_b32 v[2:3], v45 offset0:72 offset1:76
	v_add_co_u32_e32 v8, vcc, s0, v8
	s_lshl_b64 s[0:1], s[20:21], 10
	s_waitcnt lgkmcnt(1)
	v_add_f32_e32 v0, v0, v1
	s_waitcnt lgkmcnt(0)
	v_add_f32_e32 v0, v0, v2
	s_add_u32 s0, s6, s0
	v_addc_co_u32_e32 v9, vcc, 0, v9, vcc
	v_add_f32_e32 v0, v0, v3
	s_addc_u32 s1, s7, s1
	global_store_dwordx4 v[8:9], v[4:7], off
	global_store_dword v45, v0, s[0:1]
